# phase-1 epilogue: 14 v_pk_fma_f32 split into scalar v_fma_f32 pairs (bit-identical)
# speedup vs baseline: 1.0264x; 1.0014x over previous
_Z7na_mainPKDF16_PKhS0_PKfS4_S4_S4_Pf:
	s_lshl_b32 s3, s2, 5
	s_and_b32 s3, s3, 0xe0
	s_ashr_i32 s2, s2, 3
	s_add_i32 s3, s3, s2
	s_ashr_i32 s2, s3, 6
	s_lshl_b32 s3, s3, 5
	s_and_b32 s14, s3, 0x7e0
	v_mov_b32_e32 v1, 0x7c0
	s_load_dwordx8 s[4:11], s[0:1], 0x0
	s_load_dwordx2 s[18:19], s[0:1], 0x20
	s_load_dwordx2 s[28:29], s[0:1], 0x28
	s_load_dwordx2 s[34:35], s[0:1], 0x30
	s_load_dwordx2 s[30:31], s[0:1], 0x38
	v_med3_u32 v1, s14, 32, v1
	v_subrev_u32_e32 v97, 32, v1
	s_ashr_i32 s3, s2, 31
	v_lshlrev_b32_e32 v58, 1, v97
	s_lshl_b64 s[12:13], s[2:3], 12
	v_mov_b32_e32 v59, 0
	v_sub_u32_e32 v60, s14, v97
	v_lshl_add_u64 v[10:11], s[12:13], 0, v[58:59]
	v_lshlrev_b64 v[2:3], 9, v[10:11]
	v_lshl_or_b32 v22, v60, 6, v0
	s_waitcnt lgkmcnt(0)
	s_load_dword s32, s[28:29], 0x0
	v_and_b32_e32 v208, 31, v0
	v_lshlrev_b32_e32 v208, 5, v208
	global_load_dwordx4 v[192:195], v208, s[18:19]
	global_load_dwordx4 v[196:199], v208, s[18:19] offset:16
	v_lshl_add_u64 v[20:21], s[4:5], 0, v[2:3]
	v_ashrrev_i32_e32 v23, 31, v22
	v_lshl_add_u64 v[2:3], v[22:23], 4, v[20:21]
	global_load_dwordx4 v[12:15], v[2:3], off
	v_or_b32_e32 v28, 0x200, v22
	v_ashrrev_i32_e32 v29, 31, v28
	v_lshl_add_u64 v[2:3], v[28:29], 4, v[20:21]
	global_load_dwordx4 v[16:19], v[2:3], off
	v_or_b32_e32 v184, 0x400, v22
	v_ashrrev_i32_e32 v185, 31, v184
	v_lshl_add_u64 v[184:185], v[184:185], 4, v[20:21]
	v_or_b32_e32 v188, 0x600, v22
	v_ashrrev_i32_e32 v189, 31, v188
	v_lshl_add_u64 v[188:189], v[188:189], 4, v[20:21]
	global_load_dwordx4 v[184:187], v[184:185], off
	global_load_dwordx4 v[188:191], v[188:189], off
	v_lshrrev_b32_e32 v99, 6, v0
	v_and_b32_e32 v98, 63, v0
	v_lshlrev_b32_e32 v118, 13, v99
	v_lshl_or_b32 v58, v98, 4, v118
	v_and_b32_e32 v58, 0xfff0, v58
	v_add_u32_e32 v251, 0x1000, v58
	s_movk_i32 s15, 0x1000
	v_lshl_add_u64 v[24:25], s[6:7], 0, v[58:59]
	v_or_b32_e32 v32, 0x400, v22
	v_or_b32_e32 v62, 0x600, v22
	v_add_co_u32_e32 v64, vcc, s15, v24
	s_mov_b64 s[12:13], 0x1000
	s_mov_b64 s[16:17], 0x1800
	v_lshlrev_b32_e32 v72, 1, v60
	v_lshrrev_b32_e32 v23, 5, v22
	v_and_b32_e32 v34, 32, v22
	v_ashrrev_i32_e32 v33, 31, v32
	v_ashrrev_i32_e32 v63, 31, v62
	v_addc_co_u32_e32 v65, vcc, 0, v25, vcc
	global_load_dwordx4 v[6:9], v58, s[6:7] offset:1024
	global_load_dwordx4 v[2:5], v58, s[6:7]
	global_load_dwordx4 v[54:57], v58, s[6:7] offset:3072
	global_load_dwordx4 v[50:53], v58, s[6:7] offset:2048
	v_lshrrev_b32_e32 v58, 6, v22
	v_bfe_u32 v73, v22, 8, 2
	v_lshl_add_u64 v[26:27], v[24:25], 0, s[12:13]
	v_lshl_add_u64 v[24:25], v[24:25], 0, s[16:17]
	v_cmp_ne_u32_e32 vcc, 0, v34
	v_sub_u32_e32 v75, v23, v72
	global_load_dwordx4 v[42:45], v251, s[6:7]
	global_load_dwordx4 v[46:49], v251, s[6:7] offset:1024
	global_load_dwordx4 v[34:37], v251, s[6:7] offset:2048
	global_load_dwordx4 v[38:41], v251, s[6:7] offset:3072
	v_mov_b32_e32 v61, 0x60
	v_cndmask_b32_e32 v74, 0, v61, vcc
	v_add_u32_e32 v33, v74, v58
	v_lshlrev_b32_e32 v64, 2, v33
	v_bfe_u32 v96, v0, 4, 1
	v_and_b32_e32 v100, 15, v0
	v_mov_b32_e32 v30, v59
	v_mov_b32_e32 v31, v59
	v_and_b32_e32 v64, 12, v64
	v_mul_u32_u24_e32 v29, 0xc000, v96
	v_bitop3_b32 v64, v64, v100, v73 bitop3:0x36
	v_lshl_or_b32 v64, v64, 4, v29
	v_lshlrev_b32_e32 v63, 1, v75
	v_lshl_add_u32 v33, v33, 8, v64
	v_bfe_u32 v71, v0, 1, 4
	v_and_b32_e32 v70, 32, v0
	v_lshlrev_b32_e32 v1, 3, v0
	v_lshrrev_b32_e32 v58, 1, v75
	v_and_b32_e32 v1, 8, v1
	v_add_lshl_u32 v58, v58, v70, 8
	v_lshlrev_b32_e32 v121, 3, v99
	v_bfe_u32 v101, v0, 4, 2
	v_lshlrev_b32_e32 v102, 2, v101
	v_and_b32_e32 v116, 31, v0
	v_bfe_u32 v119, v0, 5, 1
	v_lshlrev_b32_e32 v124, 1, v119
	v_lshlrev_b32_e32 v117, 8, v116
	v_lshrrev_b32_e32 v95, 4, v0
	s_movk_i32 s16, 0x60
	s_mov_b32 s17, 0xc000
	v_and_b32_e32 v211, 3, v99
	v_lshrrev_b32_e32 v212, 2, v99
	v_lshl_or_b32 v211, v211, 2, v212
	v_xor_b32_e32 v213, v100, v211
	v_mul_u32_u24_e32 v214, 0x60, v119
	v_add3_u32 v214, v214, v60, v99
	v_mul_u32_u24_e32 v215, 0xc000, v96
	v_lshl_add_u32 v214, v214, 8, v215
	v_lshl_or_b32 v220, v213, 4, v214
	v_xor_b32_e32 v221, 32, v220
	v_xor_b32_e32 v216, v71, v211
	v_lshl_add_u32 v217, v119, 5, v99
	v_lshlrev_b32_e32 v217, 8, v217
	v_lshl_or_b32 v216, v216, 4, v217
	v_or_b32_e32 v216, v216, v1
	v_add_u32_e32 v222, 0x23800, v216
	v_xor_b32_e32 v223, 32, v222
	s_waitcnt vmcnt(11)
	ds_write_b128 v220, v[12:15]
	v_fma_mix_f32 v200, v192, v12, 0 op_sel_hi:[0,1,0]
	v_fma_mix_f32 v201, v193, v12, 0 op_sel:[0,1,0] op_sel_hi:[0,1,0]
	v_cvt_f32_f16_e32 v211, v12
	v_cvt_f32_f16_sdwa v212, v12 dst_sel:DWORD dst_unused:UNUSED_PAD src0_sel:WORD_1
	v_fma_mix_f32 v200, v194, v13, v200 op_sel_hi:[0,1,0]
	v_fma_mix_f32 v201, v195, v13, v201 op_sel:[0,1,0] op_sel_hi:[0,1,0]
	v_cvt_f32_f16_e32 v213, v13
	v_cvt_f32_f16_sdwa v214, v13 dst_sel:DWORD dst_unused:UNUSED_PAD src0_sel:WORD_1
	v_fma_mix_f32 v200, v196, v14, v200 op_sel_hi:[0,1,0]
	v_fma_mix_f32 v201, v197, v14, v201 op_sel:[0,1,0] op_sel_hi:[0,1,0]
	v_cvt_f32_f16_e32 v215, v14
	v_cvt_f32_f16_sdwa v216, v14 dst_sel:DWORD dst_unused:UNUSED_PAD src0_sel:WORD_1
	v_fma_mix_f32 v200, v198, v15, v200 op_sel_hi:[0,1,0]
	v_fma_mix_f32 v201, v199, v15, v201 op_sel:[0,1,0] op_sel_hi:[0,1,0]
	v_cvt_f32_f16_e32 v217, v15
	v_cvt_f32_f16_sdwa v218, v15 dst_sel:DWORD dst_unused:UNUSED_PAD src0_sel:WORD_1
	v_cvt_pk_fp8_f32 v224, v211, v212
	v_cvt_pk_fp8_f32 v225, v215, v216
	v_cvt_pk_fp8_f32 v224, v213, v214 op_sel:[0,0,1]
	v_cvt_pk_fp8_f32 v225, v217, v218 op_sel:[0,0,1]
	s_nop 0
	ds_write_b64 v222, v[224:225]
	s_waitcnt vmcnt(10)
	ds_write_b128 v221, v[16:19] offset:2048
	v_fma_mix_f32 v202, v192, v16, 0 op_sel_hi:[0,1,0]
	v_fma_mix_f32 v203, v193, v16, 0 op_sel:[0,1,0] op_sel_hi:[0,1,0]
	v_cvt_f32_f16_e32 v211, v16
	v_cvt_f32_f16_sdwa v212, v16 dst_sel:DWORD dst_unused:UNUSED_PAD src0_sel:WORD_1
	v_fma_mix_f32 v202, v194, v17, v202 op_sel_hi:[0,1,0]
	v_fma_mix_f32 v203, v195, v17, v203 op_sel:[0,1,0] op_sel_hi:[0,1,0]
	v_cvt_f32_f16_e32 v213, v17
	v_cvt_f32_f16_sdwa v214, v17 dst_sel:DWORD dst_unused:UNUSED_PAD src0_sel:WORD_1
	v_fma_mix_f32 v202, v196, v18, v202 op_sel_hi:[0,1,0]
	v_fma_mix_f32 v203, v197, v18, v203 op_sel:[0,1,0] op_sel_hi:[0,1,0]
	v_cvt_f32_f16_e32 v215, v18
	v_cvt_f32_f16_sdwa v216, v18 dst_sel:DWORD dst_unused:UNUSED_PAD src0_sel:WORD_1
	v_fma_mix_f32 v202, v198, v19, v202 op_sel_hi:[0,1,0]
	v_fma_mix_f32 v203, v199, v19, v203 op_sel:[0,1,0] op_sel_hi:[0,1,0]
	v_cvt_f32_f16_e32 v217, v19
	v_cvt_f32_f16_sdwa v218, v19 dst_sel:DWORD dst_unused:UNUSED_PAD src0_sel:WORD_1
	v_cvt_pk_fp8_f32 v226, v211, v212
	v_cvt_pk_fp8_f32 v227, v215, v216
	v_cvt_pk_fp8_f32 v226, v213, v214 op_sel:[0,0,1]
	v_cvt_pk_fp8_f32 v227, v217, v218 op_sel:[0,0,1]
	s_nop 0
	ds_write_b64 v223, v[226:227] offset:2048
	s_waitcnt vmcnt(9)
	ds_write_b128 v220, v[184:187] offset:4096
	v_fma_mix_f32 v204, v192, v184, 0 op_sel_hi:[0,1,0]
	v_fma_mix_f32 v205, v193, v184, 0 op_sel:[0,1,0] op_sel_hi:[0,1,0]
	v_cvt_f32_f16_e32 v211, v184
	v_cvt_f32_f16_sdwa v212, v184 dst_sel:DWORD dst_unused:UNUSED_PAD src0_sel:WORD_1
	v_fma_mix_f32 v204, v194, v185, v204 op_sel_hi:[0,1,0]
	v_fma_mix_f32 v205, v195, v185, v205 op_sel:[0,1,0] op_sel_hi:[0,1,0]
	v_cvt_f32_f16_e32 v213, v185
	v_cvt_f32_f16_sdwa v214, v185 dst_sel:DWORD dst_unused:UNUSED_PAD src0_sel:WORD_1
	v_fma_mix_f32 v204, v196, v186, v204 op_sel_hi:[0,1,0]
	v_fma_mix_f32 v205, v197, v186, v205 op_sel:[0,1,0] op_sel_hi:[0,1,0]
	v_cvt_f32_f16_e32 v215, v186
	v_cvt_f32_f16_sdwa v216, v186 dst_sel:DWORD dst_unused:UNUSED_PAD src0_sel:WORD_1
	v_fma_mix_f32 v204, v198, v187, v204 op_sel_hi:[0,1,0]
	v_fma_mix_f32 v205, v199, v187, v205 op_sel:[0,1,0] op_sel_hi:[0,1,0]
	v_cvt_f32_f16_e32 v217, v187
	v_cvt_f32_f16_sdwa v218, v187 dst_sel:DWORD dst_unused:UNUSED_PAD src0_sel:WORD_1
	v_cvt_pk_fp8_f32 v228, v211, v212
	v_cvt_pk_fp8_f32 v229, v215, v216
	v_cvt_pk_fp8_f32 v228, v213, v214 op_sel:[0,0,1]
	v_cvt_pk_fp8_f32 v229, v217, v218 op_sel:[0,0,1]
	s_nop 0
	ds_write_b64 v222, v[228:229] offset:4096
	s_waitcnt vmcnt(8)
	ds_write_b128 v221, v[188:191] offset:6144
	v_fma_mix_f32 v206, v192, v188, 0 op_sel_hi:[0,1,0]
	v_fma_mix_f32 v207, v193, v188, 0 op_sel:[0,1,0] op_sel_hi:[0,1,0]
	v_cvt_f32_f16_e32 v211, v188
	v_cvt_f32_f16_sdwa v212, v188 dst_sel:DWORD dst_unused:UNUSED_PAD src0_sel:WORD_1
	v_fma_mix_f32 v206, v194, v189, v206 op_sel_hi:[0,1,0]
	v_fma_mix_f32 v207, v195, v189, v207 op_sel:[0,1,0] op_sel_hi:[0,1,0]
	v_cvt_f32_f16_e32 v213, v189
	v_cvt_f32_f16_sdwa v214, v189 dst_sel:DWORD dst_unused:UNUSED_PAD src0_sel:WORD_1
	v_fma_mix_f32 v206, v196, v190, v206 op_sel_hi:[0,1,0]
	v_fma_mix_f32 v207, v197, v190, v207 op_sel:[0,1,0] op_sel_hi:[0,1,0]
	v_cvt_f32_f16_e32 v215, v190
	v_cvt_f32_f16_sdwa v216, v190 dst_sel:DWORD dst_unused:UNUSED_PAD src0_sel:WORD_1
	v_fma_mix_f32 v206, v198, v191, v206 op_sel_hi:[0,1,0]
	v_fma_mix_f32 v207, v199, v191, v207 op_sel:[0,1,0] op_sel_hi:[0,1,0]
	v_cvt_f32_f16_e32 v217, v191
	v_cvt_f32_f16_sdwa v218, v191 dst_sel:DWORD dst_unused:UNUSED_PAD src0_sel:WORD_1
	v_cvt_pk_fp8_f32 v230, v211, v212
	v_cvt_pk_fp8_f32 v231, v215, v216
	v_cvt_pk_fp8_f32 v230, v213, v214 op_sel:[0,0,1]
	v_cvt_pk_fp8_f32 v231, v217, v218 op_sel:[0,0,1]
	s_nop 0
	ds_write_b64 v223, v[230:231] offset:6144
	v_add_f32_e32 v200, v200, v201
	v_add_f32_e32 v202, v202, v203
	v_add_f32_e32 v204, v204, v205
	v_add_f32_e32 v206, v206, v207
	v_lshlrev_b32_e32 v208, 7, v119
	v_lshl_add_u32 v208, v99, 2, v208
	v_add_u32_e32 v208, 0x27800, v208
	v_add_f32_dpp v200, v200, v200 quad_perm:[1,0,3,2] row_mask:0xf bank_mask:0xf
	v_add_f32_dpp v202, v202, v202 quad_perm:[1,0,3,2] row_mask:0xf bank_mask:0xf
	v_add_f32_dpp v204, v204, v204 quad_perm:[1,0,3,2] row_mask:0xf bank_mask:0xf
	v_add_f32_dpp v206, v206, v206 quad_perm:[1,0,3,2] row_mask:0xf bank_mask:0xf
	v_add_f32_dpp v200, v200, v200 quad_perm:[2,3,0,1] row_mask:0xf bank_mask:0xf
	v_add_f32_dpp v202, v202, v202 quad_perm:[2,3,0,1] row_mask:0xf bank_mask:0xf
	v_add_f32_dpp v204, v204, v204 quad_perm:[2,3,0,1] row_mask:0xf bank_mask:0xf
	v_add_f32_dpp v206, v206, v206 quad_perm:[2,3,0,1] row_mask:0xf bank_mask:0xf
	v_add_f32_dpp v200, v200, v200 row_half_mirror row_mask:0xf bank_mask:0xf
	v_add_f32_dpp v202, v202, v202 row_half_mirror row_mask:0xf bank_mask:0xf
	v_add_f32_dpp v204, v204, v204 row_half_mirror row_mask:0xf bank_mask:0xf
	v_add_f32_dpp v206, v206, v206 row_half_mirror row_mask:0xf bank_mask:0xf
	v_add_f32_dpp v200, v200, v200 row_mirror row_mask:0xf bank_mask:0xf
	v_add_f32_dpp v202, v202, v202 row_mirror row_mask:0xf bank_mask:0xf
	v_add_f32_dpp v204, v204, v204 row_mirror row_mask:0xf bank_mask:0xf
	v_add_f32_dpp v206, v206, v206 row_mirror row_mask:0xf bank_mask:0xf
	v_add_f32_dpp v200, v200, v200 row_bcast:15 row_mask:0xa bank_mask:0xf
	v_add_f32_dpp v202, v202, v202 row_bcast:15 row_mask:0xa bank_mask:0xf
	v_add_f32_dpp v204, v204, v204 row_bcast:15 row_mask:0xa bank_mask:0xf
	v_add_f32_dpp v206, v206, v206 row_bcast:15 row_mask:0xa bank_mask:0xf
	s_mov_b32 exec_lo, 0xffff0000
	s_mov_b32 exec_hi, 0xffff0000
	ds_write_b32 v208, v200
	ds_write_b32 v208, v202 offset:32
	ds_write_b32 v208, v204 offset:64
	ds_write_b32 v208, v206 offset:96
	s_mov_b64 exec, -1
	v_lshlrev_b32_e32 v201, 7, v99
	v_lshl_or_b32 v201, v119, 4, v201
	global_load_dwordx4 v[184:187], v201, s[10:11]
	global_load_dwordx4 v[188:191], v201, s[10:11] offset:32
	global_load_dwordx4 v[192:195], v201, s[10:11] offset:64
	global_load_dwordx4 v[196:199], v201, s[10:11] offset:96
	v_cmp_lt_i32_e32 vcc, v121, v60
	s_nop 0
	v_mov_b32_e32 v15, v59
	v_cndmask_b32_e64 v12, 32, 0, vcc
	v_add_u32_e32 v16, v12, v121
	v_or_b32_e32 v12, v16, v101
	v_lshlrev_b32_e32 v58, 1, v12
	v_lshrrev_b32_e32 v12, 5, v0
	v_and_b32_e32 v12, 2, v12
	v_bitop3_b32 v14, v102, v100, v12 bitop3:0x36
	v_lshl_add_u64 v[12:13], v[10:11], 0, v[58:59]
	v_lshlrev_b64 v[12:13], 9, v[12:13]
	v_lshlrev_b32_e32 v16, 8, v16
	v_lshl_add_u64 v[12:13], s[4:5], 0, v[12:13]
	v_lshlrev_b32_e32 v14, 4, v14
	v_readfirstlane_b32 s6, v16
	v_add_u32_e32 v17, 0xc000, v16
	v_lshl_add_u64 v[12:13], v[12:13], 0, v[14:15]
	s_mov_b32 m0, s6
	s_mov_b64 s[6:7], 0x100
	v_readfirstlane_b32 s12, v17
	global_load_lds_dwordx4 v[12:13], off
	v_lshl_add_u64 v[12:13], v[12:13], 0, s[6:7]
	s_mov_b32 m0, s12
	v_or_b32_e32 v58, 1, v58
	global_load_lds_dwordx4 v[12:13], off
	v_lshl_add_u64 v[12:13], v[10:11], 0, v[58:59]
	v_lshlrev_b64 v[12:13], 9, v[12:13]
	v_lshl_add_u64 v[12:13], s[4:5], 0, v[12:13]
	v_lshl_add_u64 v[12:13], v[12:13], 0, v[14:15]
	v_add_u32_e32 v14, 0x6000, v16
	v_bfe_u32 v61, v0, 2, 2
	v_readfirstlane_b32 s12, v14
	v_add_u32_e32 v14, 0x12000, v16
	s_mov_b32 m0, s12
	v_readfirstlane_b32 s12, v14
	global_load_lds_dwordx4 v[12:13], off
	v_lshl_add_u64 v[12:13], v[12:13], 0, s[6:7]
	s_mov_b32 m0, s12
	v_add_u32_e32 v18, 0x23800, v117
	global_load_lds_dwordx4 v[12:13], off
	v_or_b32_e32 v12, 4, v121
	v_cmp_lt_i32_e32 vcc, v12, v60
	s_nop 1
	v_cndmask_b32_e64 v13, 32, 0, vcc
	v_add_u32_e32 v16, v13, v12
	v_or_b32_e32 v13, v16, v101
	v_lshlrev_b32_e32 v58, 1, v13
	v_bfe_u32 v12, v12, 2, 2
	v_bitop3_b32 v14, v102, v100, v12 bitop3:0x36
	v_lshl_add_u64 v[12:13], v[10:11], 0, v[58:59]
	v_lshlrev_b64 v[12:13], 9, v[12:13]
	v_lshlrev_b32_e32 v16, 8, v16
	v_lshl_add_u64 v[12:13], s[4:5], 0, v[12:13]
	v_lshlrev_b32_e32 v14, 4, v14
	v_readfirstlane_b32 s12, v16
	v_add_u32_e32 v17, 0xc000, v16
	v_lshl_add_u64 v[12:13], v[12:13], 0, v[14:15]
	s_mov_b32 m0, s12
	v_readfirstlane_b32 s12, v17
	v_or_b32_e32 v58, 1, v58
	global_load_lds_dwordx4 v[12:13], off
	v_lshl_add_u64 v[12:13], v[12:13], 0, s[6:7]
	s_mov_b32 m0, s12
	v_lshl_add_u64 v[10:11], v[10:11], 0, v[58:59]
	global_load_lds_dwordx4 v[12:13], off
	v_lshlrev_b64 v[10:11], 9, v[10:11]
	v_add_u32_e32 v12, 0x6000, v16
	v_lshl_add_u64 v[10:11], s[4:5], 0, v[10:11]
	v_readfirstlane_b32 s4, v12
	v_add_u32_e32 v12, 0x12000, v16
	v_lshl_add_u64 v[10:11], v[10:11], 0, v[14:15]
	s_mov_b32 m0, s4
	v_readfirstlane_b32 s4, v12
	global_load_lds_dwordx4 v[10:11], off
	v_lshl_add_u64 v[10:11], v[10:11], 0, s[6:7]
	s_mov_b32 m0, s4
	s_nop 0
	global_load_lds_dwordx4 v[10:11], off
	s_waitcnt lgkmcnt(0)
	s_barrier
	v_lshlrev_b32_e32 v10, 2, v0
	v_and_b32_e32 v94, 12, v10
	v_or_b32_e32 v120, v94, v61
	v_bitop3_b32 v10, v124, v94, v61 bitop3:0x1e
	v_lshl_or_b32 v14, v10, 4, v18
	v_bitop3_b32 v10, v124, v120, 1 bitop3:0x36
	v_lshl_or_b32 v19, v10, 4, v18
	ds_read_b128 v[10:13], v14
	ds_read_b128 v[62:65], v14 offset:8192
	ds_read_b128 v[14:17], v19
	ds_read_b128 v[66:69], v19 offset:8192
	v_bitop3_b32 v19, v124, v120, 4 bitop3:0x36
	v_lshl_or_b32 v19, v19, 4, v18
	v_bitop3_b32 v20, v124, v120, 5 bitop3:0x36
	v_lshl_or_b32 v20, v20, 4, v18
	ds_read_b128 v[70:73], v19
	ds_read_b128 v[78:81], v19 offset:8192
	ds_read_b128 v[74:77], v20
	ds_read_b128 v[82:85], v20 offset:8192
	v_bitop3_b32 v19, v124, v120, 8 bitop3:0x36
	v_lshl_or_b32 v19, v19, 4, v18
	v_bitop3_b32 v20, v124, v120, 9 bitop3:0x36
	v_lshl_or_b32 v20, v20, 4, v18
	ds_read_b128 v[86:89], v19
	ds_read_b128 v[104:107], v19 offset:8192
	ds_read_b128 v[90:93], v20
	ds_read_b128 v[108:111], v20 offset:8192
	v_bitop3_b32 v19, v124, v120, 12 bitop3:0x36
	v_lshl_or_b32 v19, v19, 4, v18
	v_bitop3_b32 v20, v124, v120, 13 bitop3:0x36
	v_lshl_or_b32 v18, v20, 4, v18
	ds_read_b128 v[126:129], v19
	ds_read_b128 v[134:137], v19 offset:8192
	ds_read_b128 v[130:133], v18
	ds_read_b128 v[138:141], v18 offset:8192
	v_mov_b32_e32 v103, 0x7f
	v_lshlrev_b32_e32 v58, 7, v99
	v_or_b32_e32 v122, 0x18000, v117
	s_waitcnt vmcnt(18) lgkmcnt(0)
	v_mfma_scale_f32_32x32x64_f8f6f4 v[18:33], v[2:9], v[10:17], 0, v103, v103 op_sel_hi:[0,0,0]
	v_lshlrev_b32_e32 v125, 3, v119
	v_or_b32_e32 v123, 0x1a000, v117
	v_mfma_scale_f32_32x32x64_f8f6f4 v[2:17], v[2:9], v[62:69], 0, v103, v103 op_sel_hi:[0,0,0]
	v_and_b32_e32 v62, 12, v95
	s_waitcnt vmcnt(16)
	v_mfma_scale_f32_32x32x64_f8f6f4 v[18:33], v[50:57], v[70:77], v[18:33], v103, v103 op_sel_hi:[0,0,0]
	v_mfma_scale_f32_32x32x64_f8f6f4 v[2:17], v[50:57], v[78:85], v[2:17], v103, v103 op_sel_hi:[0,0,0]
	s_brev_b32 s10, 60
	v_lshlrev_b32_e32 v58, 6, v0
	v_and_b32_e32 v58, 0x4000, v58
	v_or3_b32 v63, v122, v58, v125
	v_or3_b32 v58, v123, v58, v125
	s_waitcnt vmcnt(14)
	v_mfma_scale_f32_32x32x64_f8f6f4 v[18:33], v[42:49], v[86:93], v[18:33], v103, v103 op_sel_hi:[0,0,0]
	v_mfma_scale_f32_32x32x64_f8f6f4 v[2:17], v[42:49], v[104:111], v[2:17], v103, v103 op_sel_hi:[0,0,0]
	s_nop 0
	s_waitcnt vmcnt(12)
	v_mfma_scale_f32_32x32x64_f8f6f4 v[2:17], v[34:41], v[134:141], v[2:17], v103, v103 op_sel_hi:[0,0,0]
	v_mfma_scale_f32_32x32x64_f8f6f4 v[18:33], v[34:41], v[126:133], v[18:33], v103, v103 op_sel_hi:[0,0,0]
	s_waitcnt vmcnt(8)
	s_nop 15
	s_nop 1
	v_fma_f32 v2, v2, s10, v184
	v_fma_f32 v3, v3, s10, v185
	v_fma_f32 v4, v4, s10, v186
	v_fma_f32 v5, v5, s10, v187
	v_cvt_pk_f16_f32 v2, v2, v3
	v_cvt_pk_f16_f32 v3, v4, v5
	v_bitop3_b32 v4, v95, v120, 12 bitop3:0x6c
	v_fma_f32 v18, v18, s10, v184
	v_fma_f32 v19, v19, s10, v185
	v_fma_f32 v20, v20, s10, v186
	v_fma_f32 v21, v21, s10, v187
	v_lshlrev_b32_e32 v4, 4, v4
	v_cvt_pk_f16_f32 v18, v18, v19
	v_cvt_pk_f16_f32 v19, v20, v21
	v_or_b32_e32 v5, v63, v4
	v_or_b32_e32 v4, v58, v4
	ds_write_b64 v5, v[18:19]
	ds_write_b64 v4, v[2:3]
	v_fma_f32 v2, v22, s10, v188
	v_fma_f32 v3, v23, s10, v189
	v_fma_f32 v4, v6, s10, v188
	v_fma_f32 v5, v7, s10, v189
	v_fma_f32 v6, v24, s10, v190
	v_fma_f32 v7, v25, s10, v191
	v_cvt_pk_f16_f32 v2, v2, v3
	v_cvt_pk_f16_f32 v3, v6, v7
	v_fma_f32 v6, v8, s10, v190
	v_fma_f32 v7, v9, s10, v191
	v_cvt_pk_f16_f32 v4, v4, v5
	v_cvt_pk_f16_f32 v5, v6, v7
	v_bitop3_b32 v6, v62, v120, 1 bitop3:0x36
	v_lshlrev_b32_e32 v6, 4, v6
	v_or_b32_e32 v7, v63, v6
	ds_write_b64 v7, v[2:3]
	v_or_b32_e32 v2, v58, v6
	ds_write_b64 v2, v[4:5]
	v_fma_f32 v2, v26, s10, v192
	v_fma_f32 v3, v27, s10, v193
	v_fma_f32 v6, v28, s10, v194
	v_fma_f32 v7, v29, s10, v195
	v_cvt_pk_f16_f32 v2, v2, v3
	v_fma_f32 v4, v10, s10, v192
	v_fma_f32 v5, v11, s10, v193
	v_cvt_pk_f16_f32 v3, v6, v7
	v_fma_f32 v6, v12, s10, v194
	v_fma_f32 v7, v13, s10, v195
	v_cvt_pk_f16_f32 v4, v4, v5
	v_cvt_pk_f16_f32 v5, v6, v7
	v_bitop3_b32 v6, v62, v120, 2 bitop3:0x36
	v_lshlrev_b32_e32 v6, 4, v6
	v_or_b32_e32 v7, v63, v6
	ds_write_b64 v7, v[2:3]
	v_or_b32_e32 v2, v58, v6
	ds_write_b64 v2, v[4:5]
	v_fma_f32 v2, v30, s10, v196
	v_fma_f32 v3, v31, s10, v197
	v_fma_f32 v6, v32, s10, v198
	v_fma_f32 v7, v33, s10, v199
	v_cvt_pk_f16_f32 v2, v2, v3
	v_fma_f32 v4, v14, s10, v196
	v_fma_f32 v5, v15, s10, v197
	v_cvt_pk_f16_f32 v3, v6, v7
	v_fma_f32 v6, v16, s10, v198
	v_fma_f32 v7, v17, s10, v199
	v_cvt_pk_f16_f32 v4, v4, v5
	v_cvt_pk_f16_f32 v5, v6, v7
	v_bitop3_b32 v6, v62, v120, 3 bitop3:0x36
	v_lshlrev_b32_e32 v6, 4, v6
	v_or_b32_e32 v7, v63, v6
	ds_write_b64 v7, v[2:3]
	v_or_b32_e32 v2, v58, v6
	ds_write_b64 v2, v[4:5]
	s_waitcnt vmcnt(0) lgkmcnt(0)
	s_barrier
	v_and_b32_e32 v236, 1, v101
	v_lshrrev_b32_e32 v237, 1, v101
	v_xor_b32_e32 v237, v237, v236
	v_lshl_or_b32 v236, v236, 1, v237
	v_lshrrev_b32_e32 v27, 8, v0
	v_lshrrev_b32_e32 v3, 3, v0
	v_and_b32_e32 v3, 16, v3
	v_mul_u32_u24_e32 v28, 0x60, v27
	v_lshlrev_b32_e32 v26, 5, v27
	v_or_b32_e32 v146, v3, v100
	v_or_b32_e32 v147, v28, v100
	v_or_b32_e32 v4, v146, v26
	v_lshlrev_b32_e32 v209, 2, v4
	v_add_u32_e32 v209, 0x27800, v209
	v_lshlrev_b32_e32 v4, 8, v4
	v_or_b32_e32 v5, 0x18000, v4
	v_bitop3_b32 v11, v236, v120, 12 bitop3:0x36
	v_or_b32_e32 v95, 0x1c000, v4
	v_lshlrev_b32_e32 v29, 3, v101
	v_bitop3_b32 v6, v236, v94, v61 bitop3:0x1e
	v_bitop3_b32 v8, v236, v120, 4 bitop3:0x36
	v_bitop3_b32 v10, v236, v120, 8 bitop3:0x36
	v_lshlrev_b32_e32 v94, 4, v11
	v_lshlrev_b32_e32 v6, 4, v6
	v_lshlrev_b32_e32 v8, 4, v8
	v_lshlrev_b32_e32 v58, 4, v10
	v_or_b32_e32 v7, v5, v6
	v_or_b32_e32 v9, v5, v8
	v_or_b32_e32 v10, v5, v58
	v_or_b32_e32 v5, v5, v94
	v_or_b32_e32 v6, v95, v6
	v_or_b32_e32 v60, v95, v8
	ds_read_b128 v[22:25], v7
	ds_read_b128 v[18:21], v9
	ds_read_b128 v[14:17], v10
	ds_read_b128 v[10:13], v5
	ds_read_b128 v[6:9], v6
	ds_read_b128 v[2:5], v60
	v_bfe_u32 v103, v0, 6, 1
	s_movk_i32 s5, 0x2000
	v_mad_u32_u24 v44, v103, 48, v147
	v_lshlrev_b32_e32 v60, 8, v44
	v_lshlrev_b32_e32 v44, 2, v44
	v_or_b32_e32 v35, v95, v58
	v_lshlrev_b32_e32 v58, 14, v99
	v_and_b32_e32 v44, 12, v44
	v_or_b32_e32 v56, v44, v61
	v_bitop3_b32 v44, v236, v44, v61 bitop3:0x1e
	v_lshl_add_u64 v[32:33], s[8:9], 0, v[58:59]
	v_lshlrev_b32_e32 v58, 4, v98
	v_or_b32_e32 v36, v95, v94
	v_lshl_add_u64 v[88:89], v[32:33], 0, v[58:59]
	v_lshl_or_b32 v57, v44, 4, v60
	ds_read_b128 v[40:43], v35
	ds_read_b128 v[106:109], v36
	global_load_dwordx4 v[36:39], v[88:89], off
	global_load_dwordx4 v[32:35], v[88:89], off offset:1024
	ds_read_b128 v[44:47], v57
	v_bitop3_b32 v48, v236, v56, 4 bitop3:0x36
	v_lshl_or_b32 v62, v48, 4, v60
	ds_read_b128 v[48:51], v62
	v_bitop3_b32 v52, v236, v56, 8 bitop3:0x36
	v_lshl_or_b32 v63, v52, 4, v60
	ds_read_b128 v[52:55], v63
	s_waitcnt lgkmcnt(0)
	v_mfma_f32_16x16x32_f16 v[44:47], v[44:47], v[22:25], 0
	v_bitop3_b32 v64, v236, v56, 12 bitop3:0x36
	ds_read_b128 v[56:59], v57 offset:49152
	v_lshl_or_b32 v60, v64, 4, v60
	v_mfma_f32_16x16x32_f16 v[44:47], v[48:51], v[18:21], v[44:47]
	ds_read_b128 v[68:71], v60
	ds_read_b128 v[72:75], v62 offset:49152
	v_mad_u32_u24 v104, v103, 3, 1
	v_lshlrev_b32_e32 v132, 4, v104
	v_mfma_f32_16x16x32_f16 v[44:47], v[52:55], v[14:17], v[44:47]
	v_add_u32_e32 v52, v132, v147
	global_load_dwordx4 v[64:67], v[88:89], off offset:2048
	global_load_dwordx4 v[48:51], v[88:89], off offset:3072
	ds_read_b128 v[76:79], v63 offset:49152
	ds_read_b128 v[80:83], v60 offset:49152
	s_waitcnt lgkmcnt(3)
	v_mfma_f32_16x16x32_f16 v[44:47], v[68:71], v[10:13], v[44:47]
	v_lshlrev_b32_e32 v60, 8, v52
	v_lshlrev_b32_e32 v52, 2, v52
	v_and_b32_e32 v52, 12, v52
	v_mfma_f32_16x16x32_f16 v[44:47], v[56:59], v[6:9], v[44:47]
	v_or_b32_e32 v62, v52, v61
	v_bitop3_b32 v52, v236, v52, v61 bitop3:0x1e
	v_lshl_or_b32 v63, v52, 4, v60
	s_waitcnt lgkmcnt(2)
	v_mfma_f32_16x16x32_f16 v[44:47], v[72:75], v[2:5], v[44:47]
	ds_read_b128 v[52:55], v63
	v_bitop3_b32 v56, v236, v62, 4 bitop3:0x36
	v_lshl_or_b32 v84, v56, 4, v60
	s_waitcnt lgkmcnt(2)
	v_mfma_f32_16x16x32_f16 v[44:47], v[76:79], v[40:43], v[44:47]
	ds_read_b128 v[56:59], v84
	v_bitop3_b32 v68, v236, v62, 8 bitop3:0x36
	v_lshl_or_b32 v85, v68, 4, v60
	s_waitcnt lgkmcnt(2)
	v_mfma_f32_16x16x32_f16 v[110:113], v[80:83], v[106:109], v[44:47]
	ds_read_b128 v[68:71], v63 offset:49152
	v_bitop3_b32 v62, v236, v62, 12 bitop3:0x36
	v_lshl_or_b32 v60, v62, 4, v60
	ds_read_b128 v[44:47], v85
	s_waitcnt lgkmcnt(3)
	v_mfma_f32_16x16x32_f16 v[52:55], v[52:55], v[22:25], 0
	ds_read_b128 v[72:75], v60
	ds_read_b128 v[76:79], v84 offset:49152
	v_mad_u32_u24 v105, v103, 3, 2
	v_lshlrev_b32_e32 v133, 4, v105
	s_waitcnt lgkmcnt(4)
	v_mfma_f32_16x16x32_f16 v[52:55], v[56:59], v[18:21], v[52:55]
	ds_read_b128 v[56:59], v85 offset:49152
	v_add_co_u32_e32 v114, vcc, s15, v88
	s_waitcnt lgkmcnt(3)
	v_mfma_f32_16x16x32_f16 v[44:47], v[44:47], v[14:17], v[52:55]
	v_addc_co_u32_e32 v115, vcc, 0, v89, vcc
	s_waitcnt lgkmcnt(2)
	v_mfma_f32_16x16x32_f16 v[44:47], v[72:75], v[10:13], v[44:47]
	ds_read_b128 v[52:55], v60 offset:49152
	v_add_u32_e32 v60, v133, v147
	v_lshlrev_b32_e32 v72, 8, v60
	v_lshlrev_b32_e32 v60, 2, v60
	v_mfma_f32_16x16x32_f16 v[44:47], v[68:71], v[6:9], v[44:47]
	v_and_b32_e32 v60, 12, v60
	v_or_b32_e32 v68, v60, v61
	v_bitop3_b32 v60, v236, v60, v61 bitop3:0x1e
	v_lshl_or_b32 v69, v60, 4, v72
	s_waitcnt lgkmcnt(2)
	v_mfma_f32_16x16x32_f16 v[44:47], v[76:79], v[2:5], v[44:47]
	ds_read_b128 v[60:63], v69
	v_bitop3_b32 v70, v236, v68, 4 bitop3:0x36
	v_lshl_or_b32 v70, v70, 4, v72
	s_waitcnt lgkmcnt(2)
	v_mfma_f32_16x16x32_f16 v[44:47], v[56:59], v[40:43], v[44:47]
	ds_read_b128 v[56:59], v70
	v_bitop3_b32 v71, v236, v68, 8 bitop3:0x36
	v_lshl_or_b32 v71, v71, 4, v72
	s_waitcnt lgkmcnt(1)
	v_mfma_f32_16x16x32_f16 v[22:25], v[60:63], v[22:25], 0
	v_bitop3_b32 v60, v236, v68, 12 bitop3:0x36
	v_lshl_or_b32 v68, v60, 4, v72
	ds_read_b32 v210, v209
	v_mfma_f32_16x16x32_f16 v[126:129], v[52:55], v[106:109], v[44:47]
	s_nop 2
	ds_read_b128 v[44:47], v71
	ds_read_b128 v[52:55], v69 offset:49152
	ds_read_b128 v[60:63], v70 offset:49152
	s_waitcnt lgkmcnt(4)
	v_mfma_f32_16x16x32_f16 v[18:21], v[56:59], v[18:21], v[22:25]
	ds_read_b128 v[56:59], v71 offset:49152
	s_nop 1
	ds_read_b128 v[22:25], v68
	s_waitcnt lgkmcnt(4)
	v_mfma_f32_16x16x32_f16 v[14:17], v[44:47], v[14:17], v[18:21]
	v_add_co_u32_e32 v44, vcc, s5, v88
	s_movk_i32 s5, 0x3000
	s_nop 0
	ds_read_b128 v[18:21], v68 offset:49152
	s_waitcnt lgkmcnt(1)
	v_mfma_f32_16x16x32_f16 v[10:13], v[22:25], v[10:13], v[14:17]
	v_addc_co_u32_e32 v45, vcc, 0, v89, vcc
	global_load_dwordx4 v[84:87], v[114:115], off offset:1024
	global_load_dwordx4 v[80:83], v[114:115], off offset:2048
	global_load_dwordx4 v[92:95], v[44:45], off offset:-4096
	global_load_dwordx4 v[76:79], v[44:45], off
	v_mfma_f32_16x16x32_f16 v[6:9], v[52:55], v[6:9], v[10:13]
	global_load_dwordx4 v[72:75], v[44:45], off offset:1024
	global_load_dwordx4 v[68:71], v[44:45], off offset:2048
	global_load_dwordx4 v[52:55], v[44:45], off offset:3072
	v_mov_b32_e32 v13, 0xff61b1e6
	v_mfma_f32_16x16x32_f16 v[2:5], v[60:63], v[2:5], v[6:9]
	s_nop 2
	v_add_co_u32_e32 v6, vcc, s5, v88
	v_mfma_f32_16x16x32_f16 v[2:5], v[56:59], v[40:43], v[2:5]
	s_nop 0
	v_addc_co_u32_e32 v7, vcc, 0, v89, vcc
	global_load_dwordx4 v[88:91], v[114:115], off offset:3072
	global_load_dwordx4 v[60:63], v[6:7], off
	global_load_dwordx4 v[56:59], v[6:7], off offset:1024
	global_load_dwordx4 v[44:47], v[6:7], off offset:2048
	global_load_dwordx4 v[40:43], v[6:7], off offset:3072
	s_waitcnt lgkmcnt(0)
	v_mfma_f32_16x16x32_f16 v[16:19], v[18:21], v[106:109], v[2:5]
	s_mov_b32 s5, 0xff61b1e6
	s_nop 0
	v_or_b32_e32 v3, s14, v146
	v_mov_b32_e32 v4, 0x7df
	v_med3_u32 v3, v3, 32, v4
	v_or_b32_e32 v4, v97, v102
	v_sub_u32_e32 v3, v4, v3
	v_add_f32_e32 v2, s32, v210
	v_add_u32_e32 v3, 32, v3
	v_mad_u32_u24 v4, v103, 48, v3
	s_movk_i32 s4, 0x41
	v_add_f32_e32 v5, v2, v110
	v_mul_f32_e32 v5, 0x3db8aa3b, v5
	v_cmp_gt_u32_e32 vcc, s4, v4
	v_add_u32_e32 v6, 1, v4
	v_add_f32_e32 v7, v2, v111
	v_cndmask_b32_e32 v5, v13, v5, vcc
	v_mul_f32_e32 v7, 0x3db8aa3b, v7
	v_cmp_gt_u32_e32 vcc, s4, v6
	v_add_u32_e32 v8, 2, v4
	v_add_f32_e32 v9, v2, v112
	v_cndmask_b32_e32 v6, v13, v7, vcc
	v_mul_f32_e32 v9, 0x3db8aa3b, v9
	v_cmp_gt_u32_e32 vcc, s4, v8
	v_add_u32_e32 v4, 3, v4
	v_max3_f32 v7, v5, s5, v6
	v_cndmask_b32_e32 v8, v13, v9, vcc
	v_add_f32_e32 v9, v2, v113
	v_mul_f32_e32 v9, 0x3db8aa3b, v9
	v_cmp_gt_u32_e32 vcc, s4, v4
	v_add_u32_e32 v11, v3, v132
	v_add_f32_e32 v12, v2, v127
	v_cndmask_b32_e32 v10, v13, v9, vcc
	v_max3_f32 v4, v7, v8, v10
	v_add_f32_e32 v7, v2, v126
	v_mul_f32_e32 v7, 0x3db8aa3b, v7
	v_cmp_gt_u32_e32 vcc, s4, v11
	v_add_u32_e32 v9, 1, v11
	v_mul_f32_e32 v12, 0x3db8aa3b, v12
	v_cndmask_b32_e32 v7, v13, v7, vcc
	v_cmp_gt_u32_e32 vcc, s4, v9
	v_add_f32_e32 v14, v2, v128
	v_mul_f32_e32 v14, 0x3db8aa3b, v14
	v_cndmask_b32_e32 v9, v13, v12, vcc
	v_add_u32_e32 v12, 2, v11
	v_cmp_gt_u32_e32 vcc, s4, v12
	v_add_u32_e32 v11, 3, v11
	v_add_u32_e32 v3, v3, v133
	v_cndmask_b32_e32 v12, v13, v14, vcc
	v_add_f32_e32 v14, v2, v129
	v_mul_f32_e32 v14, 0x3db8aa3b, v14
	v_cmp_gt_u32_e32 vcc, s4, v11
	v_add_f32_e32 v11, v2, v16
	v_mul_f32_e32 v11, 0x3db8aa3b, v11
	v_cndmask_b32_e32 v15, v13, v14, vcc
	v_cmp_gt_u32_e32 vcc, s4, v3
	v_add_u32_e32 v14, 1, v3
	v_add_f32_e32 v16, v2, v17
	v_cndmask_b32_e32 v11, v13, v11, vcc
	v_mul_f32_e32 v16, 0x3db8aa3b, v16
	v_cmp_gt_u32_e32 vcc, s4, v14
	v_add_f32_e32 v17, v2, v18
	v_max3_f32 v4, v4, v7, v9
	v_cndmask_b32_e32 v14, v13, v16, vcc
	v_add_u32_e32 v16, 2, v3
	v_mul_f32_e32 v17, 0x3db8aa3b, v17
	v_cmp_gt_u32_e32 vcc, s4, v16
	v_add_u32_e32 v3, 3, v3
	v_add_f32_e32 v2, v2, v19
	v_max3_f32 v4, v4, v12, v15
	v_cndmask_b32_e32 v16, v13, v17, vcc
	v_mul_f32_e32 v2, 0x3db8aa3b, v2
	v_cmp_gt_u32_e32 vcc, s4, v3
	v_max3_f32 v4, v4, v11, v14
	v_lshlrev_b32_e32 v126, 5, v99
	v_cndmask_b32_e32 v17, v13, v2, vcc
	v_max3_f32 v2, v4, v16, v17
	v_mov_b32_e32 v3, v2
	v_lshlrev_b32_e32 v127, 2, v119
	v_lshrrev_b32_e32 v4, 7, v0
	v_cmp_gt_u32_e32 vcc, 16, v98
	v_permlane16_swap_b32_e32 v3, v2
	v_max_f32_e32 v2, v2, v3
	v_mov_b32_e32 v3, v2
	s_nop 1
	v_permlane32_swap_b32_e32 v3, v2
	v_max_f32_e32 v13, v2, v3
	v_and_b32_e32 v2, 0x180, v0
	v_or_b32_e32 v2, 0x23400, v2
	v_lshlrev_b32_e32 v3, 2, v100
	s_and_saveexec_b64 s[4:5], vcc
	v_lshlrev_b32_e32 v18, 6, v103
	v_add3_u32 v18, v2, v18, v3
	ds_write_b32 v18, v13
	s_or_b64 exec, exec, s[4:5]
	v_lshlrev_b32_e32 v18, 4, v103
	v_bitop3_b32 v19, v18, 16, v100 bitop3:0x36
	v_lshl_add_u32 v2, v19, 2, v2
	s_waitcnt lgkmcnt(0)
	s_barrier
	ds_read_b32 v19, v2
	v_max_f32_e32 v13, v13, v13
	v_mul_u32_u24_e32 v20, 0xd00, v4
	v_or_b32_e32 v2, 1, v124
	s_waitcnt lgkmcnt(0)
	v_max_f32_e32 v19, v19, v19
	v_max_f32_e32 v19, v13, v19
	v_sub_f32_e32 v5, v5, v19
	v_exp_f32_e32 v5, v5
	v_sub_f32_e32 v6, v6, v19
	v_exp_f32_e32 v6, v6
	v_sub_f32_e32 v8, v8, v19
	v_mul_u32_u24_e32 v13, 0xd0, v100
	v_exp_f32_e32 v8, v8
	v_sub_f32_e32 v10, v10, v19
	v_add3_u32 v20, v13, v20, v29
	v_exp_f32_e32 v10, v10
	v_or_b32_e32 v22, 0x20000, v20
	v_add_f32_e32 v20, 0, v5
	v_add_f32_e32 v20, v20, v6
	v_add_f32_e32 v20, v20, v8
	v_add_f32_e32 v23, v20, v10
	v_cvt_pk_f16_f32 v21, v8, v10
	v_cvt_pk_f16_f32 v20, v5, v6
	v_mad_u32_u24 v5, v103, s16, v22
	ds_write_b64 v5, v[20:21]
	v_sub_f32_e32 v5, v7, v19
	v_exp_f32_e32 v5, v5
	v_sub_f32_e32 v6, v9, v19
	v_exp_f32_e32 v6, v6
	v_sub_f32_e32 v7, v12, v19
	v_exp_f32_e32 v7, v7
	v_sub_f32_e32 v8, v15, v19
	v_exp_f32_e32 v8, v8
	v_sub_f32_e32 v10, v11, v19
	v_add_f32_e32 v9, v23, v5
	v_exp_f32_e32 v10, v10
	v_sub_f32_e32 v11, v14, v19
	v_add_f32_e32 v9, v9, v6
	v_exp_f32_e32 v11, v11
	v_sub_f32_e32 v12, v16, v19
	v_add_f32_e32 v9, v9, v7
	v_exp_f32_e32 v12, v12
	v_sub_f32_e32 v14, v17, v19
	v_add_f32_e32 v9, v9, v8
	v_exp_f32_e32 v14, v14
	v_add_f32_e32 v9, v9, v10
	v_add_f32_e32 v9, v9, v11
	v_add_f32_e32 v9, v9, v12
	v_add_f32_e32 v9, v9, v14
	v_mov_b32_e32 v15, v9
	v_cvt_pk_f16_f32 v7, v7, v8
	v_cvt_pk_f16_f32 v6, v5, v6
	v_lshl_add_u32 v5, v104, 5, v22
	ds_write_b64 v5, v[6:7]
	v_permlane16_swap_b32_e32 v15, v9
	v_add_f32_e32 v5, v9, v15
	v_mov_b32_e32 v6, v5
	s_movk_i32 s7, 0xd00
	s_mov_b32 s6, 0x20000
	v_cvt_pk_f16_f32 v9, v12, v14
	v_cvt_pk_f16_f32 v8, v10, v11
	v_lshl_add_u32 v7, v105, 5, v22
	ds_write_b64 v7, v[8:9]
	v_permlane32_swap_b32_e32 v6, v5
	s_and_saveexec_b64 s[4:5], vcc
	s_cbranch_execz .LBB1_4
	v_lshlrev_b32_e32 v4, 5, v4
	v_or_b32_e32 v7, v18, v100
	v_lshlrev_b32_e32 v4, 2, v4
	v_lshlrev_b32_e32 v7, 2, v7
	s_mov_b32 s8, 0x23600
	v_add3_u32 v4, v7, v4, s8
	v_add_f32_e32 v5, v5, v6
	ds_write_b32 v4, v5
